# attention QK block: K-fragment ds_reads issued 4 steps ahead with counted lgkmcnt waits (strategy 1+8), on top of best
# speedup vs baseline: 1.0081x; 1.0043x over previous
; #define LAS __attribute__((address_space(3)))
; __device__ __forceinline__ void qkt(f32x16& p0, f32x16& p1, LAS unsigned char* lds  , int r32, int hi, const bf16x8* qr) {
;     p0 = f32x16{}; p1 = f32x16{};
;     const LAS unsigned char* kb[4];
; #pragma unroll
;     for (int dd = 0; dd < 4; ++dd) kb[dd] = lds + K_OFF + KSWZ(r32, (dd * 16 + hi * 8) * 2);
; #pragma unroll
;     for (int d0 = 0; d0 < 8; ++d0) { const LAS unsigned char* a = kb[d0 & 3] + (d0 >> 2) * 128;
;         const bf16x8 b0 = *(const LAS bf16x8*)(a);
;         const bf16x8 b1 = *(const LAS bf16x8*)(a + 32 * 256);
;         p0 = __builtin_amdgcn_mfma_f32_32x32x16_bf16(b0, qr[d0], p0, 0, 0, 0);
;         p1 = __builtin_amdgcn_mfma_f32_32x32x16_bf16(b1, qr[d0], p1, 0, 0, 0); }
; #pragma unroll
;     for (int e = 0; e < 4; ++e) { const LAS unsigned char* a = lds + P_OFF + KPSWZ(r32, (e * 2 + hi) * 16);
;         const bf16x8 b0 = *(const LAS bf16x8*)(a);
;         const bf16x8 b1 = *(const LAS bf16x8*)(a + 32 * 128);
;         p0 = __builtin_amdgcn_mfma_f32_32x32x16_bf16(b0, qr[8 + e], p0, 0, 0, 0);
;         p1 = __builtin_amdgcn_mfma_f32_32x32x16_bf16(b1, qr[8 + e], p1, 0, 0, 0); }
; }
.LBB0_720:
	s_add_i32 s4, s73, 2
	s_min_u32 s70, s4, s2
	s_lshl_b64 s[4:5], s[70:71], 18
	s_add_u32 s4, s96, s4
	s_addc_u32 s5, s97, s5
	v_lshl_add_u64 v[64:65], v[150:151], 1, s[4:5]
	s_add_i32 s8, s95, s69
	v_lshl_add_u64 v[64:65], v[64:65], 0, s[66:67]
	s_mov_b32 m0, s8
	s_waitcnt vmcnt(5)
	s_barrier
	global_load_lds_dwordx4 v[64:65], off
	v_lshl_add_u64 v[64:65], v[152:153], 1, s[4:5]
	v_lshl_add_u64 v[64:65], v[64:65], 0, s[66:67]
	s_add_i32 m0, s8, 0x2000
	s_lshl_b64 s[6:7], s[70:71], 13
	global_load_lds_dwordx4 v[64:65], off
	v_lshl_add_u64 v[64:65], v[146:147], 1, s[4:5]
	s_add_i32 m0, s8, 0x4000
	s_nop 0
	global_load_lds_dwordx4 v[64:65], off
	v_lshl_add_u64 v[64:65], v[148:149], 1, s[4:5]
	s_add_i32 m0, s8, 0x6000
	s_sub_i32 s4, s94, 63
	global_load_lds_dwordx4 v[64:65], off
	v_lshl_add_u64 v[64:65], v[154:155], 0, s[6:7]
	s_add_i32 m0, s8, 0x8000
	s_cmp_gt_i32 s4, s68
	global_load_lds_dwordx4 v[64:65], off
	s_cbranch_scc1 .LBB0_728
	s_add_i32 s4, s72, 0
	v_add_u32_e32 v216, s4, v160
	v_add_u32_e32 v220, s4, v166
	v_add_u32_e32 v217, v216, v162
	v_add_u32_e32 v218, v216, v163
	v_add_u32_e32 v219, v216, v165
	v_add_u32_e32 v216, v216, v161
	v_add_u32_e32 v221, v220, v168
	v_add_u32_e32 v222, v220, v169
	v_add_u32_e32 v223, v220, v170
	v_add_u32_e32 v220, v220, v167
	ds_read_b128 v[176:179], v216 offset:16384
	ds_read_b128 v[180:183], v216 offset:24576
	ds_read_b128 v[184:187], v217 offset:16384
	ds_read_b128 v[188:191], v217 offset:24576
	ds_read_b128 v[192:195], v218 offset:16384
	ds_read_b128 v[196:199], v218 offset:24576
	ds_read_b128 v[200:203], v219 offset:16384
	ds_read_b128 v[204:207], v219 offset:24576
	s_cmp_le_i32 s94, s33
	ds_read_b128 v[208:211], v216 offset:16512
	ds_read_b128 v[212:215], v216 offset:24704
	s_waitcnt lgkmcnt(8)
	v_mfma_f32_32x32x16_bf16 v[80:95], v[176:179], v[124:127], 0
	v_mfma_f32_32x32x16_bf16 v[64:79], v[180:183], v[124:127], 0
	ds_read_b128 v[176:179], v217 offset:16512
	ds_read_b128 v[180:183], v217 offset:24704
	s_waitcnt lgkmcnt(8)
	v_mfma_f32_32x32x16_bf16 v[80:95], v[184:187], v[100:103], v[80:95]
	v_mfma_f32_32x32x16_bf16 v[64:79], v[188:191], v[100:103], v[64:79]
	ds_read_b128 v[184:187], v218 offset:16512
	ds_read_b128 v[188:191], v218 offset:24704
	s_waitcnt lgkmcnt(8)
	v_mfma_f32_32x32x16_bf16 v[80:95], v[192:195], v[104:107], v[80:95]
	v_mfma_f32_32x32x16_bf16 v[64:79], v[196:199], v[104:107], v[64:79]
	ds_read_b128 v[192:195], v219 offset:16512
	ds_read_b128 v[196:199], v219 offset:24704
	s_waitcnt lgkmcnt(8)
	v_mfma_f32_32x32x16_bf16 v[80:95], v[200:203], v[108:111], v[80:95]
	v_mfma_f32_32x32x16_bf16 v[64:79], v[204:207], v[108:111], v[64:79]
	ds_read_b128 v[200:203], v220 offset:32768
	ds_read_b128 v[204:207], v220 offset:36864
	s_waitcnt lgkmcnt(8)
	v_mfma_f32_32x32x16_bf16 v[80:95], v[208:211], v[112:115], v[80:95]
	v_mfma_f32_32x32x16_bf16 v[64:79], v[212:215], v[112:115], v[64:79]
	ds_read_b128 v[208:211], v221 offset:32768
	ds_read_b128 v[212:215], v221 offset:36864
	s_waitcnt lgkmcnt(8)
	v_mfma_f32_32x32x16_bf16 v[80:95], v[176:179], v[116:119], v[80:95]
	v_mfma_f32_32x32x16_bf16 v[64:79], v[180:183], v[116:119], v[64:79]
	ds_read_b128 v[176:179], v222 offset:32768
	ds_read_b128 v[180:183], v222 offset:36864
	s_waitcnt lgkmcnt(8)
	v_mfma_f32_32x32x16_bf16 v[80:95], v[184:187], v[120:123], v[80:95]
	v_mfma_f32_32x32x16_bf16 v[64:79], v[188:191], v[120:123], v[64:79]
	ds_read_b128 v[184:187], v223 offset:32768
	ds_read_b128 v[188:191], v223 offset:36864
	s_waitcnt lgkmcnt(8)
	v_mfma_f32_32x32x16_bf16 v[80:95], v[192:195], v[96:99], v[80:95]
	v_mfma_f32_32x32x16_bf16 v[64:79], v[196:199], v[96:99], v[64:79]
	s_waitcnt lgkmcnt(6)
	v_mfma_f32_32x32x16_bf16 v[80:95], v[200:203], v[128:131], v[80:95]
	v_mfma_f32_32x32x16_bf16 v[64:79], v[204:207], v[128:131], v[64:79]
	s_waitcnt lgkmcnt(4)
	v_mfma_f32_32x32x16_bf16 v[80:95], v[208:211], v[136:139], v[80:95]
	v_mfma_f32_32x32x16_bf16 v[64:79], v[212:215], v[136:139], v[64:79]
	s_waitcnt lgkmcnt(2)
	v_mfma_f32_32x32x16_bf16 v[80:95], v[176:179], v[132:135], v[80:95]
	v_mfma_f32_32x32x16_bf16 v[64:79], v[180:183], v[132:135], v[64:79]
	s_waitcnt lgkmcnt(0)
	v_mfma_f32_32x32x16_bf16 v[80:95], v[184:187], v[140:143], v[80:95]
	v_mfma_f32_32x32x16_bf16 v[64:79], v[188:191], v[140:143], v[64:79]
	s_cbranch_scc1 .LBB0_723
; __device__ __forceinline__ void mask_tile(f32x16& p0, f32x16& p1, int dq) {
;     const float NEG = -__builtin_inff();
; #pragma unroll
;     for (int r = 0; r < 16; ++r) { const int c = (r & 3) + 8 * (r >> 2);
;         if (dq - c < 0) p0[r] = NEG;
;         if (dq - c - 32 < 0) p1[r] = NEG; }
; }
	v_cmp_gt_i32_e64 s[62:63], 26, v172
	v_cmp_gt_i32_e64 s[64:65], 27, v172
	v_cmp_gt_i32_e64 s[60:61], 25, v172
	s_and_b64 s[62:63], s[64:65], s[62:63]
	v_cmp_gt_i32_e64 s[58:59], 24, v172
	s_and_b64 s[60:61], s[62:63], s[60:61]
	v_cmp_gt_i32_e64 s[56:57], 19, v172
	s_and_b64 s[58:59], s[60:61], s[58:59]
	v_cmp_gt_i32_e64 s[54:55], 18, v172
	s_and_b64 s[56:57], s[58:59], s[56:57]
	v_cmp_gt_i32_e64 s[52:53], 17, v172
	s_and_b64 s[54:55], s[56:57], s[54:55]
	v_cmp_gt_i32_e64 s[50:51], 16, v172
	s_and_b64 s[52:53], s[54:55], s[52:53]
	v_cmp_gt_i32_e64 s[48:49], 11, v172
	s_and_b64 s[50:51], s[52:53], s[50:51]
	v_cmp_gt_i32_e64 s[46:47], 10, v172
	s_and_b64 s[48:49], s[50:51], s[48:49]
	v_cmp_gt_i32_e64 s[44:45], 9, v172
	s_and_b64 s[46:47], s[48:49], s[46:47]
	v_cmp_gt_i32_e64 s[42:43], 8, v172
	s_and_b64 s[44:45], s[46:47], s[44:45]
	v_cmp_gt_i32_e64 s[40:41], 3, v172
	s_and_b64 s[42:43], s[44:45], s[42:43]
	v_cmp_gt_i32_e64 s[38:39], 2, v172
	s_and_b64 s[40:41], s[42:43], s[40:41]
	v_cmp_gt_i32_e64 s[36:37], 1, v172
	s_and_b64 s[38:39], s[40:41], s[38:39]
	v_cmp_gt_i32_e64 s[34:35], 0, v172
	s_and_b64 s[36:37], s[38:39], s[36:37]
	s_and_b64 s[34:35], s[36:37], s[34:35]
	v_cmp_gt_i32_e64 s[30:31], 58, v172
	v_cndmask_b32_e64 v80, v80, v173, s[34:35]
	v_cmp_gt_i32_e64 s[34:35], 59, v172
	v_cmp_gt_i32_e64 s[28:29], 57, v172
	s_and_b64 s[30:31], s[34:35], s[30:31]
	v_cmp_gt_i32_e64 s[26:27], 56, v172
	s_and_b64 s[28:29], s[30:31], s[28:29]
	v_cmp_gt_i32_e64 s[24:25], 51, v172
	s_and_b64 s[26:27], s[28:29], s[26:27]
	v_cmp_gt_i32_e64 s[22:23], 50, v172
	s_and_b64 s[24:25], s[26:27], s[24:25]
	v_cmp_gt_i32_e64 s[20:21], 49, v172
	s_and_b64 s[22:23], s[24:25], s[22:23]
	v_cmp_gt_i32_e64 s[18:19], 48, v172
	s_and_b64 s[20:21], s[22:23], s[20:21]
	v_cmp_gt_i32_e64 s[16:17], 43, v172
	s_and_b64 s[18:19], s[20:21], s[18:19]
	v_cmp_gt_i32_e64 s[14:15], 42, v172
	s_and_b64 s[16:17], s[18:19], s[16:17]
	v_cmp_gt_i32_e64 s[12:13], 41, v172
	s_and_b64 s[14:15], s[16:17], s[14:15]
	v_cmp_gt_i32_e64 s[10:11], 40, v172
	s_and_b64 s[12:13], s[14:15], s[12:13]
	v_cmp_gt_i32_e64 s[8:9], 35, v172
	s_and_b64 s[10:11], s[12:13], s[10:11]
	v_cmp_gt_i32_e64 s[6:7], 34, v172
	s_and_b64 s[8:9], s[10:11], s[8:9]
	v_cmp_gt_i32_e64 s[4:5], 33, v172
	v_cndmask_b32_e64 v94, v94, v173, s[62:63]
	v_cndmask_b32_e64 v93, v93, v173, s[60:61]
	v_cndmask_b32_e64 v92, v92, v173, s[58:59]
	v_cndmask_b32_e64 v91, v91, v173, s[56:57]
	v_cndmask_b32_e64 v90, v90, v173, s[54:55]
	v_cndmask_b32_e64 v89, v89, v173, s[52:53]
	v_cndmask_b32_e64 v88, v88, v173, s[50:51]
	v_cndmask_b32_e64 v87, v87, v173, s[48:49]
	v_readlane_b32 s48, v254, 42
	s_and_b64 s[6:7], s[8:9], s[6:7]
	v_cmp_gt_i32_e32 vcc, 32, v172
	v_readlane_b32 s52, v254, 46
	v_readlane_b32 s53, v254, 47
	v_readlane_b32 s56, v254, 50
	v_readlane_b32 s57, v254, 51
	v_readlane_b32 s58, v254, 52
	v_readlane_b32 s59, v254, 53
	v_readlane_b32 s60, v254, 54
	v_readlane_b32 s61, v254, 55
	s_and_b64 s[4:5], s[6:7], s[4:5]
	v_readlane_b32 s62, v254, 56
	v_readlane_b32 s63, v254, 57
	s_mov_b64 s[52:53], s[56:57]
	s_mov_b64 s[56:57], s[60:61]
	s_and_b64 vcc, s[4:5], vcc
	v_cndmask_b32_e64 v95, v95, v173, s[64:65]
	s_mov_b64 s[58:59], s[62:63]
	v_cndmask_b32_e64 v86, v86, v173, s[46:47]
	v_cndmask_b32_e64 v85, v85, v173, s[44:45]
	v_cndmask_b32_e64 v84, v84, v173, s[42:43]
	v_cndmask_b32_e64 v83, v83, v173, s[40:41]
	v_cndmask_b32_e64 v82, v82, v173, s[38:39]
	v_cndmask_b32_e64 v81, v81, v173, s[36:37]
	v_cndmask_b32_e64 v79, v79, v173, s[34:35]
	v_cndmask_b32_e64 v78, v78, v173, s[30:31]
	v_cndmask_b32_e64 v77, v77, v173, s[28:29]
	v_cndmask_b32_e64 v76, v76, v173, s[26:27]
	v_cndmask_b32_e64 v75, v75, v173, s[24:25]
	v_cndmask_b32_e64 v74, v74, v173, s[22:23]
	v_cndmask_b32_e64 v73, v73, v173, s[20:21]
	v_cndmask_b32_e64 v72, v72, v173, s[18:19]
	v_cndmask_b32_e64 v71, v71, v173, s[16:17]
	v_cndmask_b32_e64 v70, v70, v173, s[14:15]
	v_cndmask_b32_e64 v69, v69, v173, s[12:13]
	v_cndmask_b32_e64 v68, v68, v173, s[10:11]
	v_cndmask_b32_e64 v67, v67, v173, s[8:9]
	v_cndmask_b32_e64 v66, v66, v173, s[6:7]
	v_cndmask_b32_e64 v65, v65, v173, s[4:5]
	v_cndmask_b32_e32 v64, v64, v173, vcc
	v_readlane_b32 s49, v254, 43
	v_readlane_b32 s50, v254, 44
	v_readlane_b32 s51, v254, 45
	v_readlane_b32 s54, v254, 48
	v_readlane_b32 s55, v254, 49
